# conv1 weights: coalesced block load staged in LDS, taps read back with ds_read2_b32 (replaces lane-strided global loads)
# baseline (speedup 1.0000x reference)
_Z12conv1_kernelPKfS0_S0_PDF16_:
	s_load_dwordx8 s[52:59], s[0:1], 0x0
	v_mul_u32_u24_e32 v1, 49, v0
	v_lshlrev_b32_e32 v10, 2, v0
	v_lshlrev_b32_e32 v58, 2, v1
	s_mul_hi_u32 s0, s2, 0xaaaaaaab
	s_waitcnt lgkmcnt(0)
	global_load_dword v1, v10, s[56:57]
	v_lshrrev_b32_e32 v54, 6, v0
	v_and_b32_e32 v55, 63, v0
	v_mul_u32_u24_e32 v54, 0x3100, v54
	v_lshl_add_u32 v54, v55, 4, v54
	v_add_u32_e32 v55, 0x1000, v54
	v_add_u32_e32 v56, 0x2000, v54
	v_add_u32_e32 v57, 0x3000, v54
	global_load_dwordx4 v[2:5], v54, s[54:55]
	global_load_dwordx4 v[6:9], v54, s[54:55] offset:1024
	global_load_dwordx4 v[10:13], v54, s[54:55] offset:2048
	global_load_dwordx4 v[14:17], v54, s[54:55] offset:3072
	global_load_dwordx4 v[18:21], v55, s[54:55]
	global_load_dwordx4 v[22:25], v55, s[54:55] offset:1024
	global_load_dwordx4 v[26:29], v55, s[54:55] offset:2048
	global_load_dwordx4 v[30:33], v55, s[54:55] offset:3072
	global_load_dwordx4 v[34:37], v56, s[54:55]
	global_load_dwordx4 v[38:41], v56, s[54:55] offset:1024
	global_load_dwordx4 v[42:45], v56, s[54:55] offset:2048
	global_load_dwordx4 v[46:49], v56, s[54:55] offset:3072
	s_mov_b64 exec, 0xffff
	global_load_dwordx4 v[50:53], v57, s[54:55]
	s_mov_b64 exec, -1
	s_lshr_b32 s33, s0, 4
	s_mov_b32 s1, 0
	s_mul_i32 s4, s33, 24
	s_mul_i32 s0, s33, 0x384
	s_mov_b32 s3, s1
	s_sub_i32 s56, s2, s4
	s_lshl_b64 s[0:1], s[0:1], 2
	s_mul_i32 s2, s56, 30
	s_add_u32 s4, s52, s0
	s_addc_u32 s5, s53, s1
	s_lshl_b64 s[0:1], s[2:3], 2
	s_add_u32 s34, s4, s0
	s_addc_u32 s35, s5, s1
	s_waitcnt vmcnt(12)
	ds_write_b128 v54, v[2:5]
	s_waitcnt vmcnt(11)
	ds_write_b128 v54, v[6:9] offset:1024
	s_waitcnt vmcnt(10)
	ds_write_b128 v54, v[10:13] offset:2048
	s_waitcnt vmcnt(9)
	ds_write_b128 v54, v[14:17] offset:3072
	s_waitcnt vmcnt(8)
	ds_write_b128 v54, v[18:21] offset:4096
	s_waitcnt vmcnt(7)
	ds_write_b128 v54, v[22:25] offset:5120
	s_waitcnt vmcnt(6)
	ds_write_b128 v54, v[26:29] offset:6144
	s_waitcnt vmcnt(5)
	ds_write_b128 v54, v[30:33] offset:7168
	s_waitcnt vmcnt(4)
	ds_write_b128 v54, v[34:37] offset:8192
	s_waitcnt vmcnt(3)
	ds_write_b128 v54, v[38:41] offset:9216
	s_waitcnt vmcnt(2)
	ds_write_b128 v54, v[42:45] offset:10240
	s_waitcnt vmcnt(1)
	ds_write_b128 v54, v[46:49] offset:11264
	s_waitcnt vmcnt(0)
	s_mov_b64 exec, 0xffff
	ds_write_b128 v54, v[50:53] offset:12288
	s_mov_b64 exec, -1
	ds_read2_b32 v[6:7], v58 offset1:1
	ds_read2_b32 v[8:9], v58 offset0:2 offset1:3
	ds_read2_b32 v[2:3], v58 offset0:4 offset1:5
	ds_read2_b32 v[4:5], v58 offset0:6 offset1:7
	ds_read2_b32 v[26:27], v58 offset0:12 offset1:13
	ds_read2_b32 v[28:29], v58 offset0:14 offset1:15
	ds_read2_b32 v[30:31], v58 offset0:8 offset1:9
	ds_read2_b32 v[32:33], v58 offset0:10 offset1:11
	s_waitcnt lgkmcnt(0)
	s_load_dwordx16 s[8:23], s[34:35], 0x0
	ds_read2_b32 v[10:11], v58 offset0:28 offset1:29
	ds_read2_b32 v[12:13], v58 offset0:30 offset1:31
	ds_read2_b32 v[14:15], v58 offset0:24 offset1:25
	ds_read2_b32 v[16:17], v58 offset0:26 offset1:27
	ds_read2_b32 v[18:19], v58 offset0:20 offset1:21
	ds_read2_b32 v[20:21], v58 offset0:22 offset1:23
	ds_read2_b32 v[22:23], v58 offset0:16 offset1:17
	ds_read2_b32 v[24:25], v58 offset0:18 offset1:19
	s_waitcnt lgkmcnt(0)
	s_load_dwordx16 s[36:51], s[34:35], 0x80
	s_mul_i32 s56, s56, 24
	s_waitcnt vmcnt(0) lgkmcnt(0)
	v_fma_f32 v37, s8, v6, v1
	v_fma_f32 v34, s9, v6, v1
	v_fma_f32 v35, s10, v6, v1
	v_fma_f32 v36, s11, v6, v1
	v_fma_f32 v38, s12, v6, v1
	v_fma_f32 v39, s13, v6, v1
	v_fma_f32 v40, s14, v6, v1
	v_fmac_f32_e32 v37, s9, v7
	v_fmac_f32_e32 v34, s10, v7
	v_fmac_f32_e32 v35, s11, v7
	v_fmac_f32_e32 v36, s12, v7
	v_fmac_f32_e32 v38, s13, v7
	v_fmac_f32_e32 v39, s14, v7
	v_fma_f32 v41, s15, v6, v1
	v_fmac_f32_e32 v40, s15, v7
	v_fmac_f32_e32 v37, s10, v8
	v_fmac_f32_e32 v34, s11, v8
	v_fmac_f32_e32 v35, s12, v8
	v_fmac_f32_e32 v36, s13, v8
	v_fmac_f32_e32 v38, s14, v8
	v_fmac_f32_e32 v39, s15, v8
	v_fma_f32 v42, s16, v6, v1
	v_fmac_f32_e32 v41, s16, v7
	v_fmac_f32_e32 v40, s16, v8
	v_fmac_f32_e32 v37, s11, v9
	v_fmac_f32_e32 v34, s12, v9
	v_fmac_f32_e32 v35, s13, v9
	v_fmac_f32_e32 v36, s14, v9
	v_fmac_f32_e32 v38, s15, v9
	v_fmac_f32_e32 v39, s16, v9
	v_fma_f32 v43, s17, v6, v1
	v_fmac_f32_e32 v42, s17, v7
	v_fmac_f32_e32 v41, s17, v8
	v_fmac_f32_e32 v40, s17, v9
	s_waitcnt lgkmcnt(0)
	v_fmac_f32_e32 v37, s12, v2
	v_fmac_f32_e32 v34, s13, v2
	v_fmac_f32_e32 v35, s14, v2
	v_fmac_f32_e32 v36, s15, v2
	v_fmac_f32_e32 v38, s16, v2
	v_fmac_f32_e32 v39, s17, v2
	v_fma_f32 v44, s18, v6, v1
	v_fmac_f32_e32 v43, s18, v7
	v_fmac_f32_e32 v42, s18, v8
	v_fmac_f32_e32 v41, s18, v9
	v_fmac_f32_e32 v40, s18, v2
	v_fmac_f32_e32 v37, s13, v3
	v_fmac_f32_e32 v34, s14, v3
	v_fmac_f32_e32 v35, s15, v3
	v_fmac_f32_e32 v36, s16, v3
	v_fmac_f32_e32 v38, s17, v3
	v_fmac_f32_e32 v39, s18, v3
	v_fma_f32 v45, s19, v6, v1
	v_fmac_f32_e32 v44, s19, v7
	v_fmac_f32_e32 v43, s19, v8
	v_fmac_f32_e32 v42, s19, v9
	v_fmac_f32_e32 v41, s19, v2
	v_fmac_f32_e32 v40, s19, v3
	v_fmac_f32_e32 v37, s14, v4
	v_fmac_f32_e32 v34, s15, v4
	v_fmac_f32_e32 v35, s16, v4
	v_fmac_f32_e32 v36, s17, v4
	v_fmac_f32_e32 v38, s18, v4
	v_fmac_f32_e32 v39, s19, v4
	s_load_dwordx16 s[4:19], s[34:35], 0x40
	v_fma_f32 v46, s20, v6, v1
	v_fma_f32 v47, s21, v6, v1
	v_fma_f32 v48, s22, v6, v1
	v_fma_f32 v49, s23, v6, v1
	s_waitcnt lgkmcnt(0)
	v_fma_f32 v50, s4, v6, v1
	v_fma_f32 v51, s5, v6, v1
	v_fma_f32 v52, s6, v6, v1
	v_fma_f32 v53, s7, v6, v1
	v_fma_f32 v54, s8, v6, v1
	v_fma_f32 v55, s9, v6, v1
	v_fmac_f32_e32 v45, s20, v7
	v_fmac_f32_e32 v46, s21, v7
	v_fmac_f32_e32 v47, s22, v7
	v_fmac_f32_e32 v48, s23, v7
	v_fmac_f32_e32 v49, s4, v7
	v_fmac_f32_e32 v50, s5, v7
	v_fmac_f32_e32 v51, s6, v7
	v_fmac_f32_e32 v52, s7, v7
	v_fmac_f32_e32 v53, s8, v7
	v_fmac_f32_e32 v54, s9, v7
	v_fma_f32 v56, s10, v6, v1
	v_fmac_f32_e32 v55, s10, v7
	v_fmac_f32_e32 v44, s20, v8
	v_fmac_f32_e32 v45, s21, v8
	v_fmac_f32_e32 v46, s22, v8
	v_fmac_f32_e32 v47, s23, v8
	v_fmac_f32_e32 v48, s4, v8
	v_fmac_f32_e32 v49, s5, v8
	v_fmac_f32_e32 v50, s6, v8
	v_fmac_f32_e32 v51, s7, v8
	v_fmac_f32_e32 v52, s8, v8
	v_fmac_f32_e32 v53, s9, v8
	v_fmac_f32_e32 v54, s10, v8
	v_fmac_f32_e32 v1, s11, v6
	v_fmac_f32_e32 v56, s11, v7
	v_fmac_f32_e32 v55, s11, v8
	v_fmac_f32_e32 v43, s20, v9
	v_fmac_f32_e32 v44, s21, v9
	v_fmac_f32_e32 v45, s22, v9
	v_fmac_f32_e32 v46, s23, v9
	v_fmac_f32_e32 v47, s4, v9
	v_fmac_f32_e32 v48, s5, v9
	v_fmac_f32_e32 v49, s6, v9
	v_fmac_f32_e32 v50, s7, v9
	v_fmac_f32_e32 v51, s8, v9
	v_fmac_f32_e32 v52, s9, v9
	v_fmac_f32_e32 v53, s10, v9
	v_fmac_f32_e32 v54, s11, v9
	v_fmac_f32_e32 v1, s12, v7
	v_fmac_f32_e32 v56, s12, v8
	v_fmac_f32_e32 v55, s12, v9
	v_fmac_f32_e32 v42, s20, v2
	v_fmac_f32_e32 v43, s21, v2
	v_fmac_f32_e32 v44, s22, v2
	v_fmac_f32_e32 v45, s23, v2
	v_fmac_f32_e32 v46, s4, v2
	v_fmac_f32_e32 v47, s5, v2
	v_fmac_f32_e32 v48, s6, v2
	v_fmac_f32_e32 v49, s7, v2
	v_fmac_f32_e32 v50, s8, v2
	v_fmac_f32_e32 v51, s9, v2
	v_fmac_f32_e32 v52, s10, v2
	v_fmac_f32_e32 v53, s11, v2
	v_fmac_f32_e32 v54, s12, v2
	v_fmac_f32_e32 v1, s13, v8
	v_fmac_f32_e32 v56, s13, v9
	v_fmac_f32_e32 v55, s13, v2
	v_fmac_f32_e32 v41, s20, v3
	v_fmac_f32_e32 v42, s21, v3
	v_fmac_f32_e32 v43, s22, v3
	v_fmac_f32_e32 v44, s23, v3
	v_fmac_f32_e32 v45, s4, v3
	v_fmac_f32_e32 v46, s5, v3
	v_fmac_f32_e32 v47, s6, v3
	v_fmac_f32_e32 v48, s7, v3
	v_fmac_f32_e32 v49, s8, v3
	v_fmac_f32_e32 v50, s9, v3
	v_fmac_f32_e32 v51, s10, v3
	v_fmac_f32_e32 v52, s11, v3
	v_fmac_f32_e32 v53, s12, v3
	v_fmac_f32_e32 v54, s13, v3
	v_fmac_f32_e32 v1, s14, v9
	v_fmac_f32_e32 v56, s14, v2
	v_fmac_f32_e32 v55, s14, v3
	v_fmac_f32_e32 v40, s20, v4
	v_fmac_f32_e32 v41, s21, v4
	v_fmac_f32_e32 v42, s22, v4
	v_fmac_f32_e32 v43, s23, v4
	v_fmac_f32_e32 v44, s4, v4
	v_fmac_f32_e32 v45, s5, v4
	v_fmac_f32_e32 v46, s6, v4
	v_fmac_f32_e32 v47, s7, v4
	v_fmac_f32_e32 v48, s8, v4
	v_fmac_f32_e32 v49, s9, v4
	v_fmac_f32_e32 v50, s10, v4
	v_fmac_f32_e32 v51, s11, v4
	v_fmac_f32_e32 v52, s12, v4
	v_fmac_f32_e32 v53, s13, v4
	v_fmac_f32_e32 v54, s14, v4
	v_fmac_f32_e32 v1, s15, v2
	v_fmac_f32_e32 v56, s15, v3
	v_fmac_f32_e32 v55, s15, v4
	s_load_dwordx16 s[0:15], s[34:35], 0xc0
	v_fmac_f32_e32 v37, s18, v5
	v_fmac_f32_e32 v34, s19, v5
	v_fmac_f32_e32 v35, s36, v5
	v_fmac_f32_e32 v36, s37, v5
	v_fmac_f32_e32 v38, s38, v5
	v_fmac_f32_e32 v39, s39, v5
	v_fmac_f32_e32 v40, s40, v5
	v_fmac_f32_e32 v41, s41, v5
	v_fmac_f32_e32 v42, s42, v5
	v_fmac_f32_e32 v43, s43, v5
	v_fmac_f32_e32 v44, s44, v5
	v_fmac_f32_e32 v45, s45, v5
	v_fmac_f32_e32 v46, s46, v5
	s_waitcnt lgkmcnt(0)
	v_fmac_f32_e32 v37, s19, v30
	v_fmac_f32_e32 v34, s36, v30
	v_fmac_f32_e32 v35, s37, v30
	v_fmac_f32_e32 v36, s38, v30
	v_fmac_f32_e32 v38, s39, v30
	v_fmac_f32_e32 v39, s40, v30
	v_fmac_f32_e32 v40, s41, v30
	v_fmac_f32_e32 v41, s42, v30
	v_fmac_f32_e32 v42, s43, v30
	v_fmac_f32_e32 v43, s44, v30
	v_fmac_f32_e32 v44, s45, v30
	v_fmac_f32_e32 v45, s46, v30
	v_fmac_f32_e32 v1, s16, v3
	v_fmac_f32_e32 v47, s47, v5
	v_fmac_f32_e32 v37, s36, v31
	v_fmac_f32_e32 v34, s37, v31
	v_fmac_f32_e32 v35, s38, v31
	v_fmac_f32_e32 v36, s39, v31
	v_fmac_f32_e32 v38, s40, v31
	v_fmac_f32_e32 v39, s41, v31
	v_fmac_f32_e32 v40, s42, v31
	v_fmac_f32_e32 v41, s43, v31
	v_fmac_f32_e32 v42, s44, v31
	v_fmac_f32_e32 v43, s45, v31
	v_fmac_f32_e32 v44, s46, v31
	v_fmac_f32_e32 v46, s47, v30
	v_fmac_f32_e32 v45, s47, v31
	v_fmac_f32_e32 v56, s16, v4
	v_fmac_f32_e32 v1, s17, v4
	v_fmac_f32_e32 v48, s48, v5
	v_fmac_f32_e32 v37, s37, v32
	v_fmac_f32_e32 v34, s38, v32
	v_fmac_f32_e32 v35, s39, v32
	v_fmac_f32_e32 v36, s40, v32
	v_fmac_f32_e32 v38, s41, v32
	v_fmac_f32_e32 v39, s42, v32
	v_fmac_f32_e32 v40, s43, v32
	v_fmac_f32_e32 v41, s44, v32
	v_fmac_f32_e32 v42, s45, v32
	v_fmac_f32_e32 v43, s46, v32
	v_fmac_f32_e32 v44, s47, v32
	v_fmac_f32_e32 v47, s48, v30
	v_fmac_f32_e32 v46, s48, v31
	v_fmac_f32_e32 v45, s48, v32
	v_fmac_f32_e32 v49, s49, v5
	v_fmac_f32_e32 v50, s50, v5
	v_fmac_f32_e32 v51, s51, v5
	s_waitcnt lgkmcnt(0)
	v_fmac_f32_e32 v52, s0, v5
	v_fmac_f32_e32 v53, s1, v5
	v_fmac_f32_e32 v54, s2, v5
	v_fmac_f32_e32 v55, s3, v5
	v_fmac_f32_e32 v56, s4, v5
	v_fmac_f32_e32 v1, s5, v5
	v_fmac_f32_e32 v37, s38, v33
	v_fmac_f32_e32 v34, s39, v33
	v_fmac_f32_e32 v35, s40, v33
	v_fmac_f32_e32 v36, s41, v33
	v_fmac_f32_e32 v38, s42, v33
	v_fmac_f32_e32 v39, s43, v33
	v_fmac_f32_e32 v40, s44, v33
	v_fmac_f32_e32 v41, s45, v33
	v_fmac_f32_e32 v42, s46, v33
	v_fmac_f32_e32 v43, s47, v33
	v_fmac_f32_e32 v44, s48, v33
	v_fmac_f32_e32 v48, s49, v30
	v_fmac_f32_e32 v47, s49, v31
	v_fmac_f32_e32 v46, s49, v32
	v_fmac_f32_e32 v45, s49, v33
	v_fmac_f32_e32 v37, s39, v26
	v_fmac_f32_e32 v34, s40, v26
	v_fmac_f32_e32 v35, s41, v26
	v_fmac_f32_e32 v36, s42, v26
	v_fmac_f32_e32 v38, s43, v26
	v_fmac_f32_e32 v39, s44, v26
	v_fmac_f32_e32 v40, s45, v26
	v_fmac_f32_e32 v41, s46, v26
	v_fmac_f32_e32 v42, s47, v26
	v_fmac_f32_e32 v43, s48, v26
	v_fmac_f32_e32 v44, s49, v26
	v_fmac_f32_e32 v49, s50, v30
	v_fmac_f32_e32 v48, s50, v31
	v_fmac_f32_e32 v47, s50, v32
	v_fmac_f32_e32 v46, s50, v33
	v_fmac_f32_e32 v45, s50, v26
	v_fmac_f32_e32 v50, s51, v30
	v_fmac_f32_e32 v51, s0, v30
	v_fmac_f32_e32 v52, s1, v30
	v_fmac_f32_e32 v53, s2, v30
	v_fmac_f32_e32 v54, s3, v30
	v_fmac_f32_e32 v55, s4, v30
	v_fmac_f32_e32 v56, s5, v30
	v_fmac_f32_e32 v1, s6, v30
	ds_read2_b32 v[2:3], v58 offset0:44 offset1:45
	ds_read2_b32 v[4:5], v58 offset0:46 offset1:47
	ds_read2_b32 v[6:7], v58 offset0:40 offset1:41
	ds_read2_b32 v[8:9], v58 offset0:42 offset1:43
	v_fmac_f32_e32 v37, s40, v27
	v_fmac_f32_e32 v34, s41, v27
	v_fmac_f32_e32 v35, s42, v27
	v_fmac_f32_e32 v36, s43, v27
	v_fmac_f32_e32 v38, s44, v27
	v_fmac_f32_e32 v39, s45, v27
	v_fmac_f32_e32 v40, s46, v27
	v_fmac_f32_e32 v41, s47, v27
	v_fmac_f32_e32 v42, s48, v27
	v_fmac_f32_e32 v43, s49, v27
	v_fmac_f32_e32 v44, s50, v27
	v_fmac_f32_e32 v49, s51, v31
	v_fmac_f32_e32 v48, s51, v32
	v_fmac_f32_e32 v47, s51, v33
	v_fmac_f32_e32 v46, s51, v26
	v_fmac_f32_e32 v45, s51, v27
	v_fmac_f32_e32 v50, s0, v31
	v_fmac_f32_e32 v51, s1, v31
	v_fmac_f32_e32 v52, s2, v31
	v_fmac_f32_e32 v53, s3, v31
	v_fmac_f32_e32 v54, s4, v31
	v_fmac_f32_e32 v55, s5, v31
	v_fmac_f32_e32 v56, s6, v31
	v_fmac_f32_e32 v1, s7, v31
	s_load_dwordx16 s[16:31], s[34:35], 0x100
	s_load_dwordx16 s[36:51], s[34:35], 0x140
	v_fmac_f32_e32 v49, s0, v32
	v_fmac_f32_e32 v50, s1, v32
	v_fmac_f32_e32 v51, s2, v32
	v_fmac_f32_e32 v52, s3, v32
	v_fmac_f32_e32 v53, s4, v32
	v_fmac_f32_e32 v54, s5, v32
	v_fmac_f32_e32 v55, s6, v32
	v_fmac_f32_e32 v56, s7, v32
	v_fmac_f32_e32 v1, s8, v32
	v_fmac_f32_e32 v48, s0, v33
	v_fmac_f32_e32 v49, s1, v33
	v_fmac_f32_e32 v50, s2, v33
	v_fmac_f32_e32 v51, s3, v33
	v_fmac_f32_e32 v52, s4, v33
	v_fmac_f32_e32 v53, s5, v33
	v_fmac_f32_e32 v54, s6, v33
	v_fmac_f32_e32 v55, s7, v33
	v_fmac_f32_e32 v56, s8, v33
	v_fmac_f32_e32 v1, s9, v33
	v_fmac_f32_e32 v47, s0, v26
	v_fmac_f32_e32 v48, s1, v26
	v_fmac_f32_e32 v49, s2, v26
	v_fmac_f32_e32 v50, s3, v26
	v_fmac_f32_e32 v51, s4, v26
	v_fmac_f32_e32 v52, s5, v26
	v_fmac_f32_e32 v53, s6, v26
	v_fmac_f32_e32 v54, s7, v26
	v_fmac_f32_e32 v55, s8, v26
	v_fmac_f32_e32 v56, s9, v26
	v_fmac_f32_e32 v1, s10, v26
	v_fmac_f32_e32 v46, s0, v27
	v_fmac_f32_e32 v47, s1, v27
	v_fmac_f32_e32 v48, s2, v27
	v_fmac_f32_e32 v49, s3, v27
	v_fmac_f32_e32 v50, s4, v27
	v_fmac_f32_e32 v51, s5, v27
	v_fmac_f32_e32 v52, s6, v27
	v_fmac_f32_e32 v53, s7, v27
	v_fmac_f32_e32 v54, s8, v27
	v_fmac_f32_e32 v55, s9, v27
	v_fmac_f32_e32 v56, s10, v27
	v_fmac_f32_e32 v1, s11, v27
	v_fmac_f32_e32 v37, s12, v28
	v_fmac_f32_e32 v34, s13, v28
	v_fmac_f32_e32 v35, s14, v28
	v_fmac_f32_e32 v36, s15, v28
	s_waitcnt lgkmcnt(0)
	v_fmac_f32_e32 v38, s16, v28
	v_fmac_f32_e32 v39, s17, v28
	v_fmac_f32_e32 v40, s18, v28
	v_fmac_f32_e32 v41, s19, v28
	v_fmac_f32_e32 v42, s20, v28
	v_fmac_f32_e32 v43, s21, v28
	v_fmac_f32_e32 v44, s22, v28
	v_fmac_f32_e32 v45, s23, v28
	v_fmac_f32_e32 v46, s24, v28
	v_fmac_f32_e32 v47, s25, v28
	v_fmac_f32_e32 v48, s26, v28
	v_fmac_f32_e32 v49, s27, v28
	v_fmac_f32_e32 v50, s28, v28
	v_fmac_f32_e32 v51, s29, v28
	v_fmac_f32_e32 v52, s30, v28
	v_fmac_f32_e32 v53, s31, v28
	v_fmac_f32_e32 v54, s36, v28
	v_fmac_f32_e32 v55, s37, v28
	v_fmac_f32_e32 v56, s38, v28
	v_fmac_f32_e32 v1, s39, v28
	v_fmac_f32_e32 v37, s13, v29
	v_fmac_f32_e32 v34, s14, v29
	v_fmac_f32_e32 v35, s15, v29
	v_fmac_f32_e32 v36, s16, v29
	v_fmac_f32_e32 v38, s17, v29
	v_fmac_f32_e32 v39, s18, v29
	v_fmac_f32_e32 v40, s19, v29
	v_fmac_f32_e32 v41, s20, v29
	v_fmac_f32_e32 v42, s21, v29
	v_fmac_f32_e32 v43, s22, v29
	v_fmac_f32_e32 v44, s23, v29
	v_fmac_f32_e32 v45, s24, v29
	v_fmac_f32_e32 v46, s25, v29
	v_fmac_f32_e32 v47, s26, v29
	v_fmac_f32_e32 v48, s27, v29
	v_fmac_f32_e32 v49, s28, v29
	v_fmac_f32_e32 v50, s29, v29
	v_fmac_f32_e32 v51, s30, v29
	v_fmac_f32_e32 v52, s31, v29
	v_fmac_f32_e32 v53, s36, v29
	v_fmac_f32_e32 v54, s37, v29
	v_fmac_f32_e32 v55, s38, v29
	v_fmac_f32_e32 v56, s39, v29
	v_fmac_f32_e32 v1, s40, v29
	ds_read2_b32 v[26:27], v58 offset0:36 offset1:37
	ds_read2_b32 v[28:29], v58 offset0:38 offset1:39
	ds_read2_b32 v[30:31], v58 offset0:32 offset1:33
	ds_read2_b32 v[32:33], v58 offset0:34 offset1:35
	ds_read_b32 v57, v58 offset:192
	s_waitcnt lgkmcnt(0)
	v_fmac_f32_e32 v37, s14, v22
	v_fmac_f32_e32 v34, s15, v22
	v_fmac_f32_e32 v37, s15, v23
	v_fmac_f32_e32 v35, s16, v22
	v_fmac_f32_e32 v34, s16, v23
	v_fmac_f32_e32 v36, s17, v22
	v_fmac_f32_e32 v38, s18, v22
	v_fmac_f32_e32 v39, s19, v22
	v_fmac_f32_e32 v40, s20, v22
	v_fmac_f32_e32 v41, s21, v22
	v_fmac_f32_e32 v42, s22, v22
	v_fmac_f32_e32 v43, s23, v22
	v_fmac_f32_e32 v44, s24, v22
	v_fmac_f32_e32 v45, s25, v22
	v_fmac_f32_e32 v46, s26, v22
	v_fmac_f32_e32 v47, s27, v22
	v_fmac_f32_e32 v48, s28, v22
	v_fmac_f32_e32 v49, s29, v22
	s_load_dwordx16 s[0:15], s[34:35], 0x180
	v_fmac_f32_e32 v37, s16, v24
	v_fmac_f32_e32 v35, s17, v23
	v_fmac_f32_e32 v34, s17, v24
	v_fmac_f32_e32 v36, s18, v23
	v_fmac_f32_e32 v38, s19, v23
	v_fmac_f32_e32 v39, s20, v23
	v_fmac_f32_e32 v40, s21, v23
	v_fmac_f32_e32 v41, s22, v23
	v_fmac_f32_e32 v42, s23, v23
	v_fmac_f32_e32 v43, s24, v23
	v_fmac_f32_e32 v44, s25, v23
	v_fmac_f32_e32 v45, s26, v23
	v_fmac_f32_e32 v46, s27, v23
	v_fmac_f32_e32 v47, s28, v23
	v_fmac_f32_e32 v48, s29, v23
	v_fmac_f32_e32 v50, s30, v22
	v_fmac_f32_e32 v49, s30, v23
	v_fmac_f32_e32 v37, s17, v25
	v_fmac_f32_e32 v35, s18, v24
	v_fmac_f32_e32 v34, s18, v25
	v_fmac_f32_e32 v36, s19, v24
	v_fmac_f32_e32 v38, s20, v24
	v_fmac_f32_e32 v39, s21, v24
	v_fmac_f32_e32 v40, s22, v24
	v_fmac_f32_e32 v41, s23, v24
	v_fmac_f32_e32 v42, s24, v24
	v_fmac_f32_e32 v43, s25, v24
	v_fmac_f32_e32 v44, s26, v24
	v_fmac_f32_e32 v45, s27, v24
	v_fmac_f32_e32 v46, s28, v24
	v_fmac_f32_e32 v47, s29, v24
	v_fmac_f32_e32 v48, s30, v24
	v_fmac_f32_e32 v51, s31, v22
	v_fmac_f32_e32 v50, s31, v23
	v_fmac_f32_e32 v49, s31, v24
	v_fmac_f32_e32 v37, s18, v18
	v_fmac_f32_e32 v35, s19, v25
	v_fmac_f32_e32 v34, s19, v18
	v_fmac_f32_e32 v36, s20, v25
	v_fmac_f32_e32 v38, s21, v25
	v_fmac_f32_e32 v39, s22, v25
	v_fmac_f32_e32 v40, s23, v25
	v_fmac_f32_e32 v41, s24, v25
	v_fmac_f32_e32 v42, s25, v25
	v_fmac_f32_e32 v43, s26, v25
	v_fmac_f32_e32 v44, s27, v25
	v_fmac_f32_e32 v45, s28, v25
	v_fmac_f32_e32 v46, s29, v25
	v_fmac_f32_e32 v47, s30, v25
	v_fmac_f32_e32 v48, s31, v25
	v_fmac_f32_e32 v52, s36, v22
	v_fmac_f32_e32 v51, s36, v23
	v_fmac_f32_e32 v50, s36, v24
	v_fmac_f32_e32 v49, s36, v25
	v_fmac_f32_e32 v35, s20, v18
	v_fmac_f32_e32 v36, s21, v18
	v_fmac_f32_e32 v38, s22, v18
	v_fmac_f32_e32 v39, s23, v18
	v_fmac_f32_e32 v40, s24, v18
	v_fmac_f32_e32 v41, s25, v18
	v_fmac_f32_e32 v42, s26, v18
	v_fmac_f32_e32 v43, s27, v18
	v_fmac_f32_e32 v44, s28, v18
	v_fmac_f32_e32 v45, s29, v18
	v_fmac_f32_e32 v46, s30, v18
	v_fmac_f32_e32 v47, s31, v18
	v_fmac_f32_e32 v48, s36, v18
	v_fmac_f32_e32 v53, s37, v22
	v_fmac_f32_e32 v52, s37, v23
	v_fmac_f32_e32 v51, s37, v24
	v_fmac_f32_e32 v50, s37, v25
	v_fmac_f32_e32 v49, s37, v18
	v_fmac_f32_e32 v37, s46, v19
	v_fmac_f32_e32 v34, s47, v19
	v_fmac_f32_e32 v54, s38, v22
	v_fmac_f32_e32 v53, s38, v23
	v_fmac_f32_e32 v52, s38, v24
	v_fmac_f32_e32 v51, s38, v25
	v_fmac_f32_e32 v50, s38, v18
	v_fmac_f32_e32 v37, s47, v20
	v_fmac_f32_e32 v35, s48, v19
	v_fmac_f32_e32 v34, s48, v20
	v_fmac_f32_e32 v36, s49, v19
	v_fmac_f32_e32 v38, s50, v19
	v_fmac_f32_e32 v39, s51, v19
	s_waitcnt lgkmcnt(0)
	v_fmac_f32_e32 v40, s0, v19
	v_fmac_f32_e32 v41, s1, v19
	v_fmac_f32_e32 v42, s2, v19
	v_fmac_f32_e32 v43, s3, v19
	v_fmac_f32_e32 v44, s4, v19
	v_fmac_f32_e32 v45, s5, v19
	v_fmac_f32_e32 v46, s6, v19
	v_fmac_f32_e32 v47, s7, v19
	v_fmac_f32_e32 v48, s8, v19
	v_fmac_f32_e32 v49, s9, v19
	v_fmac_f32_e32 v55, s39, v22
	v_fmac_f32_e32 v54, s39, v23
	v_fmac_f32_e32 v53, s39, v24
	v_fmac_f32_e32 v52, s39, v25
	v_fmac_f32_e32 v51, s39, v18
	v_fmac_f32_e32 v56, s40, v22
	v_fmac_f32_e32 v1, s41, v22
	v_fmac_f32_e32 v37, s48, v21
	v_fmac_f32_e32 v35, s49, v20
	v_fmac_f32_e32 v34, s49, v21
	v_fmac_f32_e32 v36, s50, v20
	v_fmac_f32_e32 v38, s51, v20
	v_fmac_f32_e32 v39, s0, v20
	v_fmac_f32_e32 v40, s1, v20
	v_fmac_f32_e32 v41, s2, v20
	v_fmac_f32_e32 v42, s3, v20
	v_fmac_f32_e32 v43, s4, v20
	v_fmac_f32_e32 v44, s5, v20
	v_fmac_f32_e32 v45, s6, v20
	v_fmac_f32_e32 v46, s7, v20
	v_fmac_f32_e32 v47, s8, v20
	v_fmac_f32_e32 v48, s9, v20
	v_fmac_f32_e32 v50, s10, v19
	v_fmac_f32_e32 v49, s10, v20
	s_load_dwordx16 s[16:31], s[34:35], 0x1c0
	v_fmac_f32_e32 v55, s40, v23
	v_fmac_f32_e32 v54, s40, v24
	v_fmac_f32_e32 v53, s40, v25
	v_fmac_f32_e32 v52, s40, v18
	v_fmac_f32_e32 v56, s41, v23
	v_fmac_f32_e32 v1, s42, v23
	v_fmac_f32_e32 v37, s49, v14
	v_fmac_f32_e32 v35, s50, v21
	v_fmac_f32_e32 v34, s50, v14
	v_fmac_f32_e32 v36, s51, v21
	v_fmac_f32_e32 v38, s0, v21
	v_fmac_f32_e32 v39, s1, v21
	v_fmac_f32_e32 v40, s2, v21
	v_fmac_f32_e32 v41, s3, v21
	v_fmac_f32_e32 v42, s4, v21
	v_fmac_f32_e32 v43, s5, v21
	v_fmac_f32_e32 v44, s6, v21
	v_fmac_f32_e32 v45, s7, v21
	v_fmac_f32_e32 v46, s8, v21
	v_fmac_f32_e32 v47, s9, v21
	v_fmac_f32_e32 v48, s10, v21
	v_fmac_f32_e32 v51, s11, v19
	v_fmac_f32_e32 v50, s11, v20
	v_fmac_f32_e32 v49, s11, v21
	v_fmac_f32_e32 v55, s41, v24
	v_fmac_f32_e32 v54, s41, v25
	v_fmac_f32_e32 v53, s41, v18
	v_fmac_f32_e32 v56, s42, v24
	v_fmac_f32_e32 v1, s43, v24
	v_fmac_f32_e32 v37, s50, v15
	v_fmac_f32_e32 v35, s51, v14
	v_fmac_f32_e32 v34, s51, v15
	v_fmac_f32_e32 v36, s0, v14
	v_fmac_f32_e32 v38, s1, v14
	v_fmac_f32_e32 v39, s2, v14
	v_fmac_f32_e32 v40, s3, v14
	v_fmac_f32_e32 v41, s4, v14
	v_fmac_f32_e32 v42, s5, v14
	v_fmac_f32_e32 v43, s6, v14
	v_fmac_f32_e32 v44, s7, v14
	v_fmac_f32_e32 v45, s8, v14
	v_fmac_f32_e32 v46, s9, v14
	v_fmac_f32_e32 v47, s10, v14
	v_fmac_f32_e32 v48, s11, v14
	v_fmac_f32_e32 v52, s12, v19
	v_fmac_f32_e32 v51, s12, v20
	v_fmac_f32_e32 v50, s12, v21
	v_fmac_f32_e32 v49, s12, v14
	v_fmac_f32_e32 v55, s42, v25
	v_fmac_f32_e32 v54, s42, v18
	v_fmac_f32_e32 v56, s43, v25
	v_fmac_f32_e32 v1, s44, v25
	v_fmac_f32_e32 v37, s51, v16
	v_fmac_f32_e32 v35, s0, v15
	v_fmac_f32_e32 v34, s0, v16
	v_fmac_f32_e32 v36, s1, v15
	v_fmac_f32_e32 v38, s2, v15
	v_fmac_f32_e32 v39, s3, v15
	v_fmac_f32_e32 v40, s4, v15
	v_fmac_f32_e32 v41, s5, v15
	v_fmac_f32_e32 v42, s6, v15
	v_fmac_f32_e32 v43, s7, v15
	v_fmac_f32_e32 v44, s8, v15
	v_fmac_f32_e32 v45, s9, v15
	v_fmac_f32_e32 v46, s10, v15
	v_fmac_f32_e32 v47, s11, v15
	v_fmac_f32_e32 v48, s12, v15
	v_fmac_f32_e32 v53, s13, v19
	v_fmac_f32_e32 v52, s13, v20
	v_fmac_f32_e32 v51, s13, v21
	v_fmac_f32_e32 v50, s13, v14
	v_fmac_f32_e32 v49, s13, v15
	v_fmac_f32_e32 v55, s43, v18
	v_fmac_f32_e32 v56, s44, v18
	v_fmac_f32_e32 v1, s45, v18
	v_fmac_f32_e32 v37, s0, v17
	v_fmac_f32_e32 v35, s1, v16
	v_fmac_f32_e32 v34, s1, v17
	v_fmac_f32_e32 v36, s2, v16
	v_fmac_f32_e32 v38, s3, v16
	v_fmac_f32_e32 v39, s4, v16
	v_fmac_f32_e32 v40, s5, v16
	v_fmac_f32_e32 v41, s6, v16
	v_fmac_f32_e32 v42, s7, v16
	v_fmac_f32_e32 v43, s8, v16
	v_fmac_f32_e32 v44, s9, v16
	v_fmac_f32_e32 v45, s10, v16
	v_fmac_f32_e32 v46, s11, v16
	v_fmac_f32_e32 v47, s12, v16
	v_fmac_f32_e32 v48, s13, v16
	v_fmac_f32_e32 v54, s14, v19
	v_fmac_f32_e32 v53, s14, v20
	v_fmac_f32_e32 v52, s14, v21
	v_fmac_f32_e32 v51, s14, v14
	v_fmac_f32_e32 v50, s14, v15
	v_fmac_f32_e32 v49, s14, v16
	v_fmac_f32_e32 v35, s2, v17
	v_fmac_f32_e32 v36, s3, v17
	v_fmac_f32_e32 v38, s4, v17
	v_fmac_f32_e32 v39, s5, v17
	v_fmac_f32_e32 v40, s6, v17
	v_fmac_f32_e32 v41, s7, v17
	v_fmac_f32_e32 v42, s8, v17
	v_fmac_f32_e32 v43, s9, v17
	v_fmac_f32_e32 v44, s10, v17
	v_fmac_f32_e32 v45, s11, v17
	v_fmac_f32_e32 v46, s12, v17
	v_fmac_f32_e32 v47, s13, v17
	v_fmac_f32_e32 v48, s14, v17
	v_fmac_f32_e32 v55, s15, v19
	v_fmac_f32_e32 v54, s15, v20
	v_fmac_f32_e32 v53, s15, v21
	v_fmac_f32_e32 v52, s15, v14
	v_fmac_f32_e32 v51, s15, v15
	v_fmac_f32_e32 v50, s15, v16
	v_fmac_f32_e32 v49, s15, v17
	s_waitcnt lgkmcnt(0)
	v_fmac_f32_e32 v56, s16, v19
	v_fmac_f32_e32 v1, s17, v19
	v_fmac_f32_e32 v37, s24, v10
	v_fmac_f32_e32 v34, s25, v10
	s_load_dwordx16 s[0:15], s[34:35], 0x200
	v_fmac_f32_e32 v55, s16, v20
	v_fmac_f32_e32 v56, s17, v20
	v_fmac_f32_e32 v1, s18, v20
	v_fmac_f32_e32 v37, s25, v11
	v_fmac_f32_e32 v35, s26, v10
	v_fmac_f32_e32 v34, s26, v11
	v_fmac_f32_e32 v54, s16, v21
	v_fmac_f32_e32 v55, s17, v21
	v_fmac_f32_e32 v56, s18, v21
	v_fmac_f32_e32 v1, s19, v21
	v_fmac_f32_e32 v37, s26, v12
	v_fmac_f32_e32 v36, s27, v10
	v_fmac_f32_e32 v35, s27, v11
	v_fmac_f32_e32 v34, s27, v12
	v_fmac_f32_e32 v53, s16, v14
	v_fmac_f32_e32 v52, s16, v15
	v_fmac_f32_e32 v51, s16, v16
	v_fmac_f32_e32 v54, s17, v14
	v_fmac_f32_e32 v55, s18, v14
	v_fmac_f32_e32 v56, s19, v14
	v_fmac_f32_e32 v1, s20, v14
	v_fmac_f32_e32 v37, s27, v13
	v_fmac_f32_e32 v38, s28, v10
	v_fmac_f32_e32 v36, s28, v11
	v_fmac_f32_e32 v35, s28, v12
	v_fmac_f32_e32 v34, s28, v13
	v_fmac_f32_e32 v50, s16, v17
	v_fmac_f32_e32 v53, s17, v15
	v_fmac_f32_e32 v52, s17, v16
	v_fmac_f32_e32 v51, s17, v17
	v_fmac_f32_e32 v54, s18, v15
	v_fmac_f32_e32 v55, s19, v15
	v_fmac_f32_e32 v56, s20, v15
	v_fmac_f32_e32 v1, s21, v15
	s_waitcnt lgkmcnt(0)
	v_fmac_f32_e32 v37, s28, v30
	v_fmac_f32_e32 v39, s29, v10
	v_fmac_f32_e32 v38, s29, v11
	v_fmac_f32_e32 v36, s29, v12
	v_fmac_f32_e32 v35, s29, v13
	v_fmac_f32_e32 v34, s29, v30
	v_fmac_f32_e32 v53, s18, v16
	v_fmac_f32_e32 v52, s18, v17
	v_fmac_f32_e32 v54, s19, v16
	v_fmac_f32_e32 v55, s20, v16
	v_fmac_f32_e32 v56, s21, v16
	v_fmac_f32_e32 v1, s22, v16
	v_fmac_f32_e32 v37, s29, v31
	v_fmac_f32_e32 v40, s30, v10
	v_fmac_f32_e32 v39, s30, v11
	v_fmac_f32_e32 v38, s30, v12
	v_fmac_f32_e32 v36, s30, v13
	v_fmac_f32_e32 v35, s30, v30
	v_fmac_f32_e32 v34, s30, v31
	v_fmac_f32_e32 v41, s31, v10
	s_waitcnt lgkmcnt(0)
	v_fmac_f32_e32 v42, s0, v10
	v_fmac_f32_e32 v43, s1, v10
	v_fmac_f32_e32 v44, s2, v10
	v_fmac_f32_e32 v45, s3, v10
	v_fmac_f32_e32 v46, s4, v10
	v_fmac_f32_e32 v47, s5, v10
	v_fmac_f32_e32 v48, s6, v10
	v_fmac_f32_e32 v49, s7, v10
	v_fmac_f32_e32 v50, s8, v10
	v_fmac_f32_e32 v51, s9, v10
	v_fmac_f32_e32 v53, s19, v17
	v_fmac_f32_e32 v54, s20, v17
	v_fmac_f32_e32 v55, s21, v17
	v_fmac_f32_e32 v56, s22, v17
	v_fmac_f32_e32 v1, s23, v17
	v_fmac_f32_e32 v37, s30, v32
	v_fmac_f32_e32 v40, s31, v11
	v_fmac_f32_e32 v39, s31, v12
	v_fmac_f32_e32 v38, s31, v13
	v_fmac_f32_e32 v36, s31, v30
	v_fmac_f32_e32 v35, s31, v31
	v_fmac_f32_e32 v34, s31, v32
	v_fmac_f32_e32 v41, s0, v11
	v_fmac_f32_e32 v42, s1, v11
	v_fmac_f32_e32 v43, s2, v11
	v_fmac_f32_e32 v44, s3, v11
	v_fmac_f32_e32 v45, s4, v11
	v_fmac_f32_e32 v46, s5, v11
	v_fmac_f32_e32 v47, s6, v11
	v_fmac_f32_e32 v48, s7, v11
	v_fmac_f32_e32 v49, s8, v11
	v_fmac_f32_e32 v50, s9, v11
	v_fmac_f32_e32 v52, s10, v10
	v_fmac_f32_e32 v51, s10, v11
	s_load_dwordx16 s[16:31], s[34:35], 0x240
	v_fmac_f32_e32 v40, s0, v12
	v_fmac_f32_e32 v41, s1, v12
	v_fmac_f32_e32 v42, s2, v12
	v_fmac_f32_e32 v43, s3, v12
	v_fmac_f32_e32 v44, s4, v12
	v_fmac_f32_e32 v45, s5, v12
	v_fmac_f32_e32 v46, s6, v12
	v_fmac_f32_e32 v47, s7, v12
	v_fmac_f32_e32 v48, s8, v12
	v_fmac_f32_e32 v49, s9, v12
	v_fmac_f32_e32 v50, s10, v12
	v_fmac_f32_e32 v53, s11, v10
	v_fmac_f32_e32 v52, s11, v11
	v_fmac_f32_e32 v51, s11, v12
	v_fmac_f32_e32 v39, s0, v13
	v_fmac_f32_e32 v40, s1, v13
	v_fmac_f32_e32 v41, s2, v13
	v_fmac_f32_e32 v42, s3, v13
	v_fmac_f32_e32 v43, s4, v13
	v_fmac_f32_e32 v44, s5, v13
	v_fmac_f32_e32 v45, s6, v13
	v_fmac_f32_e32 v46, s7, v13
	v_fmac_f32_e32 v47, s8, v13
	v_fmac_f32_e32 v48, s9, v13
	v_fmac_f32_e32 v49, s10, v13
	v_fmac_f32_e32 v50, s11, v13
	v_fmac_f32_e32 v54, s12, v10
	v_fmac_f32_e32 v53, s12, v11
	v_fmac_f32_e32 v52, s12, v12
	v_fmac_f32_e32 v51, s12, v13
	v_fmac_f32_e32 v38, s0, v30
	v_fmac_f32_e32 v36, s0, v31
	v_fmac_f32_e32 v39, s1, v30
	v_fmac_f32_e32 v40, s2, v30
	v_fmac_f32_e32 v41, s3, v30
	v_fmac_f32_e32 v42, s4, v30
	v_fmac_f32_e32 v43, s5, v30
	v_fmac_f32_e32 v44, s6, v30
	v_fmac_f32_e32 v45, s7, v30
	v_fmac_f32_e32 v46, s8, v30
	v_fmac_f32_e32 v47, s9, v30
	v_fmac_f32_e32 v48, s10, v30
	v_fmac_f32_e32 v49, s11, v30
	v_fmac_f32_e32 v50, s12, v30
	v_fmac_f32_e32 v55, s13, v10
	v_fmac_f32_e32 v54, s13, v11
	v_fmac_f32_e32 v53, s13, v12
	v_fmac_f32_e32 v52, s13, v13
	v_fmac_f32_e32 v51, s13, v30
	v_fmac_f32_e32 v35, s0, v32
	v_fmac_f32_e32 v38, s1, v31
	v_fmac_f32_e32 v36, s1, v32
	v_fmac_f32_e32 v39, s2, v31
	v_fmac_f32_e32 v40, s3, v31
	v_fmac_f32_e32 v41, s4, v31
	v_fmac_f32_e32 v42, s5, v31
	v_fmac_f32_e32 v43, s6, v31
	v_fmac_f32_e32 v44, s7, v31
	v_fmac_f32_e32 v45, s8, v31
	v_fmac_f32_e32 v46, s9, v31
	v_fmac_f32_e32 v47, s10, v31
	v_fmac_f32_e32 v48, s11, v31
	v_fmac_f32_e32 v49, s12, v31
	v_fmac_f32_e32 v50, s13, v31
	v_fmac_f32_e32 v56, s14, v10
	v_fmac_f32_e32 v55, s14, v11
	v_fmac_f32_e32 v54, s14, v12
	v_fmac_f32_e32 v53, s14, v13
	v_fmac_f32_e32 v52, s14, v30
	v_fmac_f32_e32 v51, s14, v31
	v_fmac_f32_e32 v38, s2, v32
	v_fmac_f32_e32 v39, s3, v32
	v_fmac_f32_e32 v40, s4, v32
	v_fmac_f32_e32 v41, s5, v32
	v_fmac_f32_e32 v42, s6, v32
	v_fmac_f32_e32 v43, s7, v32
	v_fmac_f32_e32 v44, s8, v32
	v_fmac_f32_e32 v45, s9, v32
	v_fmac_f32_e32 v46, s10, v32
	v_fmac_f32_e32 v47, s11, v32
	v_fmac_f32_e32 v48, s12, v32
	v_fmac_f32_e32 v49, s13, v32
	v_fmac_f32_e32 v50, s14, v32
	v_fmac_f32_e32 v1, s15, v10
	v_fmac_f32_e32 v56, s15, v11
	v_fmac_f32_e32 v55, s15, v12
	v_fmac_f32_e32 v54, s15, v13
	v_fmac_f32_e32 v53, s15, v30
	v_fmac_f32_e32 v52, s15, v31
	v_fmac_f32_e32 v51, s15, v32
	s_waitcnt lgkmcnt(0)
	v_fmac_f32_e32 v37, s22, v33
	v_fmac_f32_e32 v34, s23, v33
	v_fmac_f32_e32 v35, s24, v33
	v_fmac_f32_e32 v36, s25, v33
	s_load_dwordx16 s[0:15], s[34:35], 0x280
	v_fmac_f32_e32 v1, s16, v11
	v_fmac_f32_e32 v37, s23, v26
	v_fmac_f32_e32 v34, s24, v26
	v_fmac_f32_e32 v35, s25, v26
	v_fmac_f32_e32 v38, s26, v33
	v_fmac_f32_e32 v36, s26, v26
	v_fmac_f32_e32 v56, s16, v12
	v_fmac_f32_e32 v1, s17, v12
	v_fmac_f32_e32 v37, s24, v27
	v_fmac_f32_e32 v34, s25, v27
	v_fmac_f32_e32 v35, s26, v27
	v_fmac_f32_e32 v39, s27, v33
	v_fmac_f32_e32 v38, s27, v26
	v_fmac_f32_e32 v36, s27, v27
	v_fmac_f32_e32 v55, s16, v13
	v_fmac_f32_e32 v54, s16, v30
	v_fmac_f32_e32 v53, s16, v31
	v_fmac_f32_e32 v56, s17, v13
	v_fmac_f32_e32 v1, s18, v13
	v_fmac_f32_e32 v37, s25, v28
	v_fmac_f32_e32 v34, s26, v28
	v_fmac_f32_e32 v35, s27, v28
	v_fmac_f32_e32 v40, s28, v33
	v_fmac_f32_e32 v39, s28, v26
	v_fmac_f32_e32 v38, s28, v27
	v_fmac_f32_e32 v36, s28, v28
	v_fmac_f32_e32 v52, s16, v32
	v_fmac_f32_e32 v55, s17, v30
	v_fmac_f32_e32 v54, s17, v31
	v_fmac_f32_e32 v53, s17, v32
	v_fmac_f32_e32 v56, s18, v30
	v_fmac_f32_e32 v1, s19, v30
	v_fmac_f32_e32 v37, s26, v29
	v_fmac_f32_e32 v34, s27, v29
	v_fmac_f32_e32 v35, s28, v29
	v_fmac_f32_e32 v41, s29, v33
	v_fmac_f32_e32 v40, s29, v26
	v_fmac_f32_e32 v39, s29, v27
	v_fmac_f32_e32 v38, s29, v28
	v_fmac_f32_e32 v36, s29, v29
	v_fmac_f32_e32 v55, s18, v31
	v_fmac_f32_e32 v54, s18, v32
	v_fmac_f32_e32 v56, s19, v31
	v_fmac_f32_e32 v1, s20, v31
	v_fmac_f32_e32 v37, s27, v6
	v_fmac_f32_e32 v34, s28, v6
	v_fmac_f32_e32 v35, s29, v6
	v_fmac_f32_e32 v42, s30, v33
	v_fmac_f32_e32 v41, s30, v26
	v_fmac_f32_e32 v40, s30, v27
	v_fmac_f32_e32 v39, s30, v28
	v_fmac_f32_e32 v38, s30, v29
	v_fmac_f32_e32 v36, s30, v6
	v_fmac_f32_e32 v43, s31, v33
	s_waitcnt lgkmcnt(0)
	v_fmac_f32_e32 v44, s0, v33
	v_fmac_f32_e32 v45, s1, v33
	v_fmac_f32_e32 v46, s2, v33
	v_fmac_f32_e32 v47, s3, v33
	v_fmac_f32_e32 v48, s4, v33
	v_fmac_f32_e32 v49, s5, v33
	v_fmac_f32_e32 v50, s6, v33
	v_fmac_f32_e32 v51, s7, v33
	v_fmac_f32_e32 v52, s8, v33
	v_fmac_f32_e32 v53, s9, v33
	v_fmac_f32_e32 v55, s19, v32
	v_fmac_f32_e32 v56, s20, v32
	v_fmac_f32_e32 v1, s21, v32
	v_fmac_f32_e32 v37, s28, v7
	v_fmac_f32_e32 v34, s29, v7
	v_fmac_f32_e32 v35, s30, v7
	v_fmac_f32_e32 v42, s31, v26
	v_fmac_f32_e32 v41, s31, v27
	v_fmac_f32_e32 v40, s31, v28
	v_fmac_f32_e32 v39, s31, v29
	v_fmac_f32_e32 v38, s31, v6
	v_fmac_f32_e32 v36, s31, v7
	v_fmac_f32_e32 v43, s0, v26
	v_fmac_f32_e32 v44, s1, v26
	v_fmac_f32_e32 v45, s2, v26
	v_fmac_f32_e32 v46, s3, v26
	v_fmac_f32_e32 v47, s4, v26
	v_fmac_f32_e32 v48, s5, v26
	v_fmac_f32_e32 v49, s6, v26
	v_fmac_f32_e32 v50, s7, v26
	v_fmac_f32_e32 v51, s8, v26
	v_fmac_f32_e32 v52, s9, v26
	v_fmac_f32_e32 v54, s10, v33
	v_fmac_f32_e32 v53, s10, v26
	s_load_dwordx16 s[16:31], s[34:35], 0x2c0
	v_fmac_f32_e32 v42, s0, v27
	v_fmac_f32_e32 v41, s0, v28
	v_fmac_f32_e32 v43, s1, v27
	v_fmac_f32_e32 v44, s2, v27
	v_fmac_f32_e32 v45, s3, v27
	v_fmac_f32_e32 v46, s4, v27
	v_fmac_f32_e32 v47, s5, v27
	v_fmac_f32_e32 v48, s6, v27
	v_fmac_f32_e32 v49, s7, v27
	v_fmac_f32_e32 v50, s8, v27
	v_fmac_f32_e32 v51, s9, v27
	v_fmac_f32_e32 v52, s10, v27
	v_fmac_f32_e32 v55, s11, v33
	v_fmac_f32_e32 v54, s11, v26
	v_fmac_f32_e32 v53, s11, v27
	v_fmac_f32_e32 v40, s0, v29
	v_fmac_f32_e32 v42, s1, v28
	v_fmac_f32_e32 v41, s1, v29
	v_fmac_f32_e32 v43, s2, v28
	v_fmac_f32_e32 v44, s3, v28
	v_fmac_f32_e32 v45, s4, v28
	v_fmac_f32_e32 v46, s5, v28
	v_fmac_f32_e32 v47, s6, v28
	v_fmac_f32_e32 v48, s7, v28
	v_fmac_f32_e32 v49, s8, v28
	v_fmac_f32_e32 v50, s9, v28
	v_fmac_f32_e32 v51, s10, v28
	v_fmac_f32_e32 v52, s11, v28
	v_fmac_f32_e32 v56, s12, v33
	v_fmac_f32_e32 v55, s12, v26
	v_fmac_f32_e32 v54, s12, v27
	v_fmac_f32_e32 v53, s12, v28
	v_fmac_f32_e32 v40, s1, v6
	v_fmac_f32_e32 v42, s2, v29
	v_fmac_f32_e32 v41, s2, v6
	v_fmac_f32_e32 v43, s3, v29
	v_fmac_f32_e32 v44, s4, v29
	v_fmac_f32_e32 v45, s5, v29
	v_fmac_f32_e32 v46, s6, v29
	v_fmac_f32_e32 v47, s7, v29
	v_fmac_f32_e32 v48, s8, v29
	v_fmac_f32_e32 v49, s9, v29
	v_fmac_f32_e32 v50, s10, v29
	v_fmac_f32_e32 v51, s11, v29
	v_fmac_f32_e32 v52, s12, v29
	v_fmac_f32_e32 v1, s13, v33
	v_fmac_f32_e32 v56, s13, v26
	v_fmac_f32_e32 v55, s13, v27
	v_fmac_f32_e32 v54, s13, v28
	v_fmac_f32_e32 v53, s13, v29
	v_fmac_f32_e32 v39, s0, v6
	v_fmac_f32_e32 v40, s2, v7
	v_fmac_f32_e32 v42, s3, v6
	v_fmac_f32_e32 v41, s3, v7
	v_fmac_f32_e32 v43, s4, v6
	v_fmac_f32_e32 v44, s5, v6
	v_fmac_f32_e32 v45, s6, v6
	v_fmac_f32_e32 v46, s7, v6
	v_fmac_f32_e32 v47, s8, v6
	v_fmac_f32_e32 v48, s9, v6
	v_fmac_f32_e32 v49, s10, v6
	v_fmac_f32_e32 v50, s11, v6
	v_fmac_f32_e32 v51, s12, v6
	v_fmac_f32_e32 v52, s13, v6
	v_fmac_f32_e32 v1, s14, v26
	v_fmac_f32_e32 v56, s14, v27
	v_fmac_f32_e32 v55, s14, v28
	v_fmac_f32_e32 v54, s14, v29
	v_fmac_f32_e32 v53, s14, v6
	v_fmac_f32_e32 v38, s0, v7
	v_fmac_f32_e32 v39, s1, v7
	v_fmac_f32_e32 v42, s4, v7
	v_fmac_f32_e32 v43, s5, v7
	v_fmac_f32_e32 v44, s6, v7
	v_fmac_f32_e32 v45, s7, v7
	v_fmac_f32_e32 v46, s8, v7
	v_fmac_f32_e32 v47, s9, v7
	v_fmac_f32_e32 v48, s10, v7
	v_fmac_f32_e32 v49, s11, v7
	v_fmac_f32_e32 v50, s12, v7
	v_fmac_f32_e32 v51, s13, v7
	v_fmac_f32_e32 v52, s14, v7
	v_fmac_f32_e32 v1, s15, v27
	v_fmac_f32_e32 v56, s15, v28
	v_fmac_f32_e32 v55, s15, v29
	v_fmac_f32_e32 v54, s15, v6
	v_fmac_f32_e32 v53, s15, v7
	s_waitcnt lgkmcnt(0)
	v_fmac_f32_e32 v40, s26, v8
	v_fmac_f32_e32 v41, s27, v8
	s_load_dwordx16 s[0:15], s[34:35], 0x300
	v_fmac_f32_e32 v40, s27, v9
	v_fmac_f32_e32 v42, s28, v8
	v_fmac_f32_e32 v41, s28, v9
	v_fmac_f32_e32 v1, s16, v28
	v_fmac_f32_e32 v56, s16, v29
	v_fmac_f32_e32 v40, s28, v2
	v_fmac_f32_e32 v43, s29, v8
	v_fmac_f32_e32 v42, s29, v9
	v_fmac_f32_e32 v41, s29, v2
	v_fmac_f32_e32 v1, s17, v29
	v_fmac_f32_e32 v56, s17, v6
	v_fmac_f32_e32 v40, s29, v3
	v_fmac_f32_e32 v44, s30, v8
	v_fmac_f32_e32 v43, s30, v9
	v_fmac_f32_e32 v42, s30, v2
	v_fmac_f32_e32 v41, s30, v3
	v_fmac_f32_e32 v1, s18, v6
	v_fmac_f32_e32 v56, s18, v7
	v_fmac_f32_e32 v40, s30, v4
	v_fmac_f32_e32 v45, s31, v8
	v_fmac_f32_e32 v44, s31, v9
	v_fmac_f32_e32 v43, s31, v2
	v_fmac_f32_e32 v42, s31, v3
	v_fmac_f32_e32 v41, s31, v4
	v_fmac_f32_e32 v55, s16, v6
	v_fmac_f32_e32 v1, s19, v7
	v_fmac_f32_e32 v40, s31, v5
	s_waitcnt lgkmcnt(0)
	v_fmac_f32_e32 v46, s0, v8
	v_fmac_f32_e32 v45, s0, v9
	v_fmac_f32_e32 v44, s0, v2
	v_fmac_f32_e32 v43, s0, v3
	v_fmac_f32_e32 v42, s0, v4
	v_fmac_f32_e32 v41, s0, v5
	v_fmac_f32_e32 v56, s10, v8
	v_fmac_f32_e32 v54, s16, v7
	v_fmac_f32_e32 v55, s17, v7
	s_waitcnt lgkmcnt(0)
	v_fmac_f32_e32 v40, s0, v57
	v_fmac_f32_e32 v47, s1, v8
	v_fmac_f32_e32 v46, s1, v9
	v_fmac_f32_e32 v45, s1, v2
	v_fmac_f32_e32 v44, s1, v3
	v_fmac_f32_e32 v43, s1, v4
	v_fmac_f32_e32 v42, s1, v5
	v_fmac_f32_e32 v41, s1, v57
	v_fmac_f32_e32 v1, s11, v8
	v_fmac_f32_e32 v56, s11, v9
	s_load_dwordx2 s[0:1], s[34:35], 0x340
	v_fmac_f32_e32 v37, s20, v8
	v_fmac_f32_e32 v34, s21, v8
	v_fmac_f32_e32 v35, s22, v8
	v_fmac_f32_e32 v36, s23, v8
	v_fmac_f32_e32 v38, s24, v8
	v_fmac_f32_e32 v39, s25, v8
	v_fmac_f32_e32 v48, s2, v8
	v_fmac_f32_e32 v49, s3, v8
	v_fmac_f32_e32 v50, s4, v8
	v_fmac_f32_e32 v51, s5, v8
	v_fmac_f32_e32 v52, s6, v8
	v_fmac_f32_e32 v53, s7, v8
	v_fmac_f32_e32 v54, s8, v8
	v_fmac_f32_e32 v55, s9, v8
	v_fmac_f32_e32 v1, s12, v9
	v_fmac_f32_e32 v56, s12, v2
	v_fmac_f32_e32 v37, s21, v9
	v_fmac_f32_e32 v34, s22, v9
	v_fmac_f32_e32 v35, s23, v9
	v_fmac_f32_e32 v36, s24, v9
	v_fmac_f32_e32 v38, s25, v9
	v_fmac_f32_e32 v39, s26, v9
	v_fmac_f32_e32 v47, s2, v9
	v_fmac_f32_e32 v48, s3, v9
	v_fmac_f32_e32 v49, s4, v9
	v_fmac_f32_e32 v50, s5, v9
	v_fmac_f32_e32 v51, s6, v9
	v_fmac_f32_e32 v52, s7, v9
	v_fmac_f32_e32 v53, s8, v9
	v_fmac_f32_e32 v54, s9, v9
	v_fmac_f32_e32 v55, s10, v9
	v_fmac_f32_e32 v1, s13, v2
	v_fmac_f32_e32 v56, s13, v3
	v_fmac_f32_e32 v37, s22, v2
	v_fmac_f32_e32 v34, s23, v2
	v_fmac_f32_e32 v35, s24, v2
	v_fmac_f32_e32 v36, s25, v2
	v_fmac_f32_e32 v38, s26, v2
	v_fmac_f32_e32 v39, s27, v2
	v_fmac_f32_e32 v46, s2, v2
	v_fmac_f32_e32 v47, s3, v2
	v_fmac_f32_e32 v48, s4, v2
	v_fmac_f32_e32 v49, s5, v2
	v_fmac_f32_e32 v50, s6, v2
	v_fmac_f32_e32 v51, s7, v2
	v_fmac_f32_e32 v52, s8, v2
	v_fmac_f32_e32 v53, s9, v2
	v_fmac_f32_e32 v54, s10, v2
	v_fmac_f32_e32 v55, s11, v2
	v_fmac_f32_e32 v1, s14, v3
	v_fmac_f32_e32 v56, s14, v4
	v_fmac_f32_e32 v37, s23, v3
	v_fmac_f32_e32 v34, s24, v3
	v_fmac_f32_e32 v35, s25, v3
	v_fmac_f32_e32 v36, s26, v3
	v_fmac_f32_e32 v38, s27, v3
	v_fmac_f32_e32 v39, s28, v3
	v_fmac_f32_e32 v45, s2, v3
	v_fmac_f32_e32 v46, s3, v3
	v_fmac_f32_e32 v47, s4, v3
	v_fmac_f32_e32 v48, s5, v3
	v_fmac_f32_e32 v49, s6, v3
	v_fmac_f32_e32 v50, s7, v3
	v_fmac_f32_e32 v51, s8, v3
	v_fmac_f32_e32 v52, s9, v3
	v_fmac_f32_e32 v53, s10, v3
	v_fmac_f32_e32 v54, s11, v3
	v_fmac_f32_e32 v55, s12, v3
	v_fmac_f32_e32 v1, s15, v4
	v_fmac_f32_e32 v56, s15, v5
	v_lshrrev_b32_e32 v2, 5, v0
	v_fmac_f32_e32 v37, s24, v4
	v_fmac_f32_e32 v34, s25, v4
	v_fmac_f32_e32 v35, s26, v4
	v_fmac_f32_e32 v36, s27, v4
	v_fmac_f32_e32 v38, s28, v4
	v_fmac_f32_e32 v39, s29, v4
	v_fmac_f32_e32 v44, s2, v4
	v_fmac_f32_e32 v45, s3, v4
	v_fmac_f32_e32 v46, s4, v4
	v_fmac_f32_e32 v47, s5, v4
	v_fmac_f32_e32 v48, s6, v4
	v_fmac_f32_e32 v49, s7, v4
	v_fmac_f32_e32 v50, s8, v4
	v_fmac_f32_e32 v51, s9, v4
	v_fmac_f32_e32 v52, s10, v4
	v_fmac_f32_e32 v53, s11, v4
	v_fmac_f32_e32 v54, s12, v4
	v_fmac_f32_e32 v55, s13, v4
	s_waitcnt lgkmcnt(0)
	v_fmac_f32_e32 v1, s0, v5
	v_fmac_f32_e32 v56, s0, v57
	v_lshl_or_b32 v4, s33, 3, v2
	v_mov_b32_e32 v2, s56
	v_mov_b32_e32 v3, 0
	s_movk_i32 s0, 0x240
	v_fmac_f32_e32 v37, s25, v5
	v_fmac_f32_e32 v34, s26, v5
	v_fmac_f32_e32 v35, s27, v5
	v_fmac_f32_e32 v36, s28, v5
	v_fmac_f32_e32 v38, s29, v5
	v_fmac_f32_e32 v39, s30, v5
	v_fmac_f32_e32 v43, s2, v5
	v_fmac_f32_e32 v44, s3, v5
	v_fmac_f32_e32 v45, s4, v5
	v_fmac_f32_e32 v46, s5, v5
	v_fmac_f32_e32 v47, s6, v5
	v_fmac_f32_e32 v48, s7, v5
	v_fmac_f32_e32 v49, s8, v5
	v_fmac_f32_e32 v50, s9, v5
	v_fmac_f32_e32 v51, s10, v5
	v_fmac_f32_e32 v52, s11, v5
	v_fmac_f32_e32 v53, s12, v5
	v_fmac_f32_e32 v54, s13, v5
	v_fmac_f32_e32 v55, s14, v5
	v_fmac_f32_e32 v1, s1, v57
	v_mad_u64_u32 v[4:5], s[0:1], v4, s0, v[2:3]
	v_fmac_f32_e32 v37, s26, v57
	v_lshlrev_b64 v[4:5], 6, v[4:5]
	v_and_b32_e32 v0, 31, v0
	v_lshl_add_u64 v[4:5], s[58:59], 0, v[4:5]
	v_lshlrev_b32_e32 v2, 1, v0
	v_max_f32_e32 v0, 0, v37
	s_mov_b32 s0, 0x42800000
	v_fmac_f32_e32 v34, s27, v57
	v_lshl_add_u64 v[2:3], v[4:5], 0, v[2:3]
	v_fma_mixlo_f16 v0, v0, s0, 0
	global_store_short v[2:3], v0, off
	v_max_f32_e32 v0, 0, v34
	v_fmac_f32_e32 v35, s28, v57
	v_fma_mixlo_f16 v0, v0, s0, 0
	global_store_short v[2:3], v0, off offset:64
	v_max_f32_e32 v0, 0, v35
	v_fmac_f32_e32 v36, s29, v57
	v_fma_mixlo_f16 v0, v0, s0, 0
	global_store_short v[2:3], v0, off offset:128
	v_max_f32_e32 v0, 0, v36
	v_fmac_f32_e32 v38, s30, v57
	v_fma_mixlo_f16 v0, v0, s0, 0
	global_store_short v[2:3], v0, off offset:192
	v_max_f32_e32 v0, 0, v38
	v_fmac_f32_e32 v39, s31, v57
	v_fma_mixlo_f16 v0, v0, s0, 0
	global_store_short v[2:3], v0, off offset:256
	v_max_f32_e32 v0, 0, v39
	v_fma_mixlo_f16 v0, v0, s0, 0
	global_store_short v[2:3], v0, off offset:320
	v_max_f32_e32 v0, 0, v40
	v_fma_mixlo_f16 v0, v0, s0, 0
	global_store_short v[2:3], v0, off offset:384
	v_max_f32_e32 v0, 0, v41
	v_fmac_f32_e32 v42, s2, v57
	v_fma_mixlo_f16 v0, v0, s0, 0
	global_store_short v[2:3], v0, off offset:448
	v_max_f32_e32 v0, 0, v42
	v_fmac_f32_e32 v43, s3, v57
	v_fma_mixlo_f16 v0, v0, s0, 0
	global_store_short v[2:3], v0, off offset:512
	v_max_f32_e32 v0, 0, v43
	v_fmac_f32_e32 v44, s4, v57
	v_fma_mixlo_f16 v0, v0, s0, 0
	global_store_short v[2:3], v0, off offset:576
	v_max_f32_e32 v0, 0, v44
	v_fmac_f32_e32 v45, s5, v57
	v_fma_mixlo_f16 v0, v0, s0, 0
	global_store_short v[2:3], v0, off offset:640
	v_max_f32_e32 v0, 0, v45
	v_fmac_f32_e32 v46, s6, v57
	v_fma_mixlo_f16 v0, v0, s0, 0
	global_store_short v[2:3], v0, off offset:704
	v_max_f32_e32 v0, 0, v46
	v_fmac_f32_e32 v47, s7, v57
	v_fma_mixlo_f16 v0, v0, s0, 0
	global_store_short v[2:3], v0, off offset:768
	v_max_f32_e32 v0, 0, v47
	v_fmac_f32_e32 v48, s8, v57
	v_fma_mixlo_f16 v0, v0, s0, 0
	global_store_short v[2:3], v0, off offset:832
	v_max_f32_e32 v0, 0, v48
	v_fmac_f32_e32 v49, s9, v57
	v_fma_mixlo_f16 v0, v0, s0, 0
	global_store_short v[2:3], v0, off offset:896
	v_max_f32_e32 v0, 0, v49
	v_fmac_f32_e32 v50, s10, v57
	v_fma_mixlo_f16 v0, v0, s0, 0
	global_store_short v[2:3], v0, off offset:960
	v_max_f32_e32 v0, 0, v50
	v_fmac_f32_e32 v51, s11, v57
	v_fma_mixlo_f16 v0, v0, s0, 0
	global_store_short v[2:3], v0, off offset:1024
	v_max_f32_e32 v0, 0, v51
	v_fmac_f32_e32 v52, s12, v57
	v_fma_mixlo_f16 v0, v0, s0, 0
	global_store_short v[2:3], v0, off offset:1088
	v_max_f32_e32 v0, 0, v52
	v_fmac_f32_e32 v53, s13, v57
	v_fma_mixlo_f16 v0, v0, s0, 0
	global_store_short v[2:3], v0, off offset:1152
	v_max_f32_e32 v0, 0, v53
	v_fmac_f32_e32 v54, s14, v57
	v_fma_mixlo_f16 v0, v0, s0, 0
	global_store_short v[2:3], v0, off offset:1216
	v_max_f32_e32 v0, 0, v54
	v_fmac_f32_e32 v55, s15, v57
	v_fma_mixlo_f16 v0, v0, s0, 0
	global_store_short v[2:3], v0, off offset:1280
	v_max_f32_e32 v0, 0, v55
	v_fma_mixlo_f16 v0, v0, s0, 0
	global_store_short v[2:3], v0, off offset:1344
	v_max_f32_e32 v0, 0, v56
	v_fma_mixlo_f16 v0, v0, s0, 0
	global_store_short v[2:3], v0, off offset:1408
	v_max_f32_e32 v0, 0, v1
	v_fma_mixlo_f16 v0, v0, s0, 0
	global_store_short v[2:3], v0, off offset:1472
	s_endpgm

	.amdhsa_kernel _Z12conv1_kernelPKfS0_S0_PDF16_
		.amdhsa_group_segment_fixed_size 50176
		.amdhsa_private_segment_fixed_size 0
		.amdhsa_kernarg_size 32
		.amdhsa_user_sgpr_count 2
		.amdhsa_user_sgpr_dispatch_ptr 0
		.amdhsa_user_sgpr_queue_ptr 0
		.amdhsa_user_sgpr_kernarg_segment_ptr 1
		.amdhsa_user_sgpr_dispatch_id 0
		.amdhsa_user_sgpr_kernarg_preload_length 0
		.amdhsa_user_sgpr_kernarg_preload_offset 0
		.amdhsa_user_sgpr_private_segment_size 0
		.amdhsa_uses_dynamic_stack 0
		.amdhsa_enable_private_segment 0
		.amdhsa_system_sgpr_workgroup_id_x 1
		.amdhsa_system_sgpr_workgroup_id_y 0
		.amdhsa_system_sgpr_workgroup_id_z 0
		.amdhsa_system_sgpr_workgroup_info 0
		.amdhsa_system_vgpr_workitem_id 0
		.amdhsa_next_free_vgpr 59
		.amdhsa_next_free_sgpr 60
		.amdhsa_accum_offset 60
		.amdhsa_reserve_vcc 0
		.amdhsa_float_round_mode_32 0
		.amdhsa_float_round_mode_16_64 0
		.amdhsa_float_denorm_mode_32 3
		.amdhsa_float_denorm_mode_16_64 3
		.amdhsa_dx10_clamp 1
		.amdhsa_ieee_mode 1
		.amdhsa_fp16_overflow 0
		.amdhsa_tg_split 0
		.amdhsa_exception_fp_ieee_invalid_op 0
		.amdhsa_exception_fp_denorm_src 0
		.amdhsa_exception_fp_ieee_div_zero 0
		.amdhsa_exception_fp_ieee_overflow 0
		.amdhsa_exception_fp_ieee_underflow 0
		.amdhsa_exception_fp_ieee_inexact 0
		.amdhsa_exception_int_div_zero 0
	.end_amdhsa_kernel

amdhsa.kernels:
  - .agpr_count:     16
    .args:
      - .address_space:  global
        .offset:         0
        .size:           8
        .value_kind:     global_buffer
      - .address_space:  global
        .offset:         8
        .size:           8
        .value_kind:     global_buffer
      - .address_space:  global
        .offset:         16
        .size:           8
        .value_kind:     global_buffer
      - .address_space:  global
        .offset:         24
        .size:           8
        .value_kind:     global_buffer
      - .address_space:  global
        .offset:         32
        .size:           8
        .value_kind:     global_buffer
      - .address_space:  global
        .offset:         40
        .size:           8
        .value_kind:     global_buffer
      - .address_space:  global
        .offset:         48
        .size:           8
        .value_kind:     global_buffer
      - .address_space:  global
        .offset:         56
        .size:           8
        .value_kind:     global_buffer
      - .address_space:  global
        .offset:         64
        .size:           8
        .value_kind:     global_buffer
      - .address_space:  global
        .offset:         72
        .size:           8
        .value_kind:     global_buffer
      - .address_space:  global
        .offset:         80
        .size:           8
        .value_kind:     global_buffer
      - .address_space:  global
        .offset:         88
        .size:           8
        .value_kind:     global_buffer
      - .address_space:  global
        .offset:         96
        .size:           8
        .value_kind:     global_buffer
      - .address_space:  global
        .offset:         104
        .size:           8
        .value_kind:     global_buffer
      - .address_space:  global
        .offset:         112
        .size:           8
        .value_kind:     global_buffer
      - .address_space:  global
        .offset:         120
        .size:           8
        .value_kind:     global_buffer
      - .address_space:  global
        .offset:         128
        .size:           8
        .value_kind:     global_buffer
      - .address_space:  global
        .offset:         136
        .size:           8
        .value_kind:     global_buffer
      - .address_space:  global
        .offset:         144
        .size:           8
        .value_kind:     global_buffer
      - .address_space:  global
        .offset:         152
        .size:           8
        .value_kind:     global_buffer
    .group_segment_fixed_size: 0
    .kernarg_segment_align: 8
    .kernarg_segment_size: 160
    .language:       OpenCL C
    .language_version:
      - 2
      - 0
    .max_flat_workgroup_size: 256
    .name:           _Z11lstm_kernelPKDF16_PKDv8_DF16_S3_S3_PKfS5_S5_S5_PDF16_S6_PfS5_PS1_PK15HIP_vector_typeIfLj4EES5_S5_S7_S5_S5_S5_
    .private_segment_fixed_size: 0
    .sgpr_count:     70
    .sgpr_spill_count: 0
    .symbol:         _Z11lstm_kernelPKDF16_PKDv8_DF16_S3_S3_PKfS5_S5_S5_PDF16_S6_PfS5_PS1_PK15HIP_vector_typeIfLj4EES5_S5_S7_S5_S5_S5_.kd
    .uniform_work_group_size: 1
    .uses_dynamic_stack: false
    .vgpr_count:     228
    .vgpr_spill_count: 0
    .wavefront_size: 64
  - .agpr_count:     0
    .args:
      - .actual_access:  read_only
        .address_space:  global
        .offset:         0
        .size:           8
        .value_kind:     global_buffer
      - .actual_access:  read_only
        .address_space:  global
        .offset:         8
        .size:           8
        .value_kind:     global_buffer
      - .actual_access:  read_only
        .address_space:  global
        .offset:         16
        .size:           8
        .value_kind:     global_buffer
      - .actual_access:  write_only
        .address_space:  global
        .offset:         24
        .size:           8
        .value_kind:     global_buffer
    .group_segment_fixed_size: 50176
    .kernarg_segment_align: 8
    .kernarg_segment_size: 32
    .language:       OpenCL C
    .language_version:
      - 2
      - 0
    .max_flat_workgroup_size: 256
    .name:           _Z12conv1_kernelPKfS0_S0_PDF16_
    .private_segment_fixed_size: 0
    .sgpr_count:     66
    .sgpr_spill_count: 0
    .symbol:         _Z12conv1_kernelPKfS0_S0_PDF16_.kd
    .uniform_work_group_size: 1
    .uses_dynamic_stack: false
    .vgpr_count:     59
    .vgpr_spill_count: 0
    .wavefront_size: 64
  - .agpr_count:     0
    .args:
      - .address_space:  global
        .offset:         0
        .size:           8
        .value_kind:     global_buffer
      - .address_space:  global
        .offset:         8
        .size:           8
        .value_kind:     global_buffer
      - .address_space:  global
        .offset:         16
        .size:           8
        .value_kind:     global_buffer
      - .address_space:  global
        .offset:         24
        .size:           8
        .value_kind:     global_buffer
      - .address_space:  global
        .offset:         32
        .size:           8
        .value_kind:     global_buffer
      - .address_space:  global
        .offset:         40
        .size:           8
        .value_kind:     global_buffer
      - .address_space:  global
        .offset:         48
        .size:           8
        .value_kind:     global_buffer
      - .address_space:  global
        .offset:         56
        .size:           8
        .value_kind:     global_buffer
      - .address_space:  global
        .offset:         64
        .size:           8
        .value_kind:     global_buffer
      - .address_space:  global
        .offset:         72
        .size:           8
        .value_kind:     global_buffer
      - .address_space:  global
        .offset:         80
        .size:           8
        .value_kind:     global_buffer
    .group_segment_fixed_size: 0
    .kernarg_segment_align: 8
    .kernarg_segment_size: 88
    .language:       OpenCL C
    .language_version:
      - 2
      - 0
    .max_flat_workgroup_size: 256
    .name:           _Z11prep_kernelPKfS0_S0_S0_PDv8_DF16_S2_S2_PKiS0_S2_PDv4_j
    .private_segment_fixed_size: 0
    .sgpr_count:     34
    .sgpr_spill_count: 0
    .symbol:         _Z11prep_kernelPKfS0_S0_S0_PDv8_DF16_S2_S2_PKiS0_S2_PDv4_j.kd
    .uniform_work_group_size: 1
    .uses_dynamic_stack: false
    .vgpr_count:     17
    .vgpr_spill_count: 0
    .wavefront_size: 64
  - .agpr_count:     104
    .args:
      - .address_space:  global
        .offset:         0
        .size:           8
        .value_kind:     global_buffer
      - .address_space:  global
        .offset:         8
        .size:           8
        .value_kind:     global_buffer
      - .address_space:  global
        .offset:         16
        .size:           8
        .value_kind:     global_buffer
      - .address_space:  global
        .offset:         24
        .size:           8
        .value_kind:     global_buffer
      - .address_space:  global
        .offset:         32
        .size:           8
        .value_kind:     global_buffer
    .group_segment_fixed_size: 129152
    .kernarg_segment_align: 8
    .kernarg_segment_size: 40
    .language:       OpenCL C
    .language_version:
      - 2
      - 0
    .max_flat_workgroup_size: 256
    .name:           _Z13pconv2_kernelPKDF16_PKDv8_DF16_PKfPfS6_
    .private_segment_fixed_size: 0
    .sgpr_count:     30
    .sgpr_spill_count: 0
    .symbol:         _Z13pconv2_kernelPKDF16_PKDv8_DF16_PKfPfS6_.kd
    .uniform_work_group_size: 1
    .uses_dynamic_stack: false
    .vgpr_count:     324
    .vgpr_spill_count: 0
    .wavefront_size: 64
  - .agpr_count:     40
    .args:
      - .address_space:  global
        .offset:         0
        .size:           8
        .value_kind:     global_buffer
      - .address_space:  global
        .offset:         8
        .size:           8
        .value_kind:     global_buffer
      - .address_space:  global
        .offset:         16
        .size:           8
        .value_kind:     global_buffer
      - .address_space:  global
        .offset:         24
        .size:           8
        .value_kind:     global_buffer
    .group_segment_fixed_size: 41472
    .kernarg_segment_align: 8
    .kernarg_segment_size: 32
    .language:       OpenCL C
    .language_version:
      - 2
      - 0
    .max_flat_workgroup_size: 256
    .name:           _Z11dcap_kernelPKfS0_S0_Pf
    .private_segment_fixed_size: 0
    .sgpr_count:     25
    .sgpr_spill_count: 0
    .symbol:         _Z11dcap_kernelPKfS0_S0_Pf.kd
    .uniform_work_group_size: 1
    .uses_dynamic_stack: false
    .vgpr_count:     244
    .vgpr_spill_count: 0
    .wavefront_size: 64
  - .agpr_count:     0
    .args:
      - .address_space:  global
        .offset:         0
        .size:           8
        .value_kind:     global_buffer
      - .address_space:  global
        .offset:         8
        .size:           8
        .value_kind:     global_buffer
    .group_segment_fixed_size: 3200
    .kernarg_segment_align: 8
    .kernarg_segment_size: 16
    .language:       OpenCL C
    .language_version:
      - 2
      - 0
    .max_flat_workgroup_size: 640
    .name:           _Z12final_kernelPKfPf
    .private_segment_fixed_size: 0
    .sgpr_count:     16
    .sgpr_spill_count: 0
    .symbol:         _Z12final_kernelPKfPf.kd
    .uniform_work_group_size: 1
    .uses_dynamic_stack: false
    .vgpr_count:     78
    .vgpr_spill_count: 0
    .wavefront_size: 64
